# P7 K-loop: LDS-DMA issue balanced 4/4/4/4 over the four load segments (B pieces 2,3 issued one segment later)
# baseline (speedup 1.0000x reference)
; #define PG8_STAGE_B(bufoff, gbase) do { _Pragma("unroll") for (int _i = 0; _i < 2; ++_i) \
;         __builtin_amdgcn_global_load_lds((const unsigned*)((const char*)(gbase) + voffB[_i]), (LAS unsigned*)(lds + (bufoff) + ldsw + _i * 8192), 16, 0, 0); } while (0)
; #define PG8_STAGE_A(bufoff, gbase, VO, h) do { _Pragma("unroll") for (int _i = 0; _i < 2; ++_i) \
;         __builtin_amdgcn_global_load_lds((const unsigned*)((const char*)(gbase) + (VO)[h][_i]), (LAS unsigned*)(lds + (bufoff) + ldsw + _i * 8192), 16, 0, 0); } while (0)
; #define PG8_WAIT_V(n) asm volatile("s_waitcnt vmcnt(" #n ")" ::: "memory")
; #define PG8_BAR __builtin_amdgcn_s_barrier()
;     ...
;     PG8_STAGE_B(PG8_SB(1, 0), cB + kstepB); PG8_STAGE_A(PG8_SA(1, 0), cA + kstep, voffA, 0); PG8_STAGE_B(PG8_SB(1, 1), cB + hstepB + kstepB);
;     PG8_WAIT_V(6); PG8_BAR;
.LBB0_1404:
	v_and_b32_e32 v1, 15, v0
	v_readlane_b32 s2, v249, 41
	v_lshrrev_b32_e32 v6, 1, v0
	v_and_b32_e32 v6, 24, v6
	v_or_b32_e32 v210, s2, v1
	v_lshlrev_b32_e32 v7, 6, v210
	v_lshlrev_b32_e32 v8, 1, v6
	s_movk_i32 s2, 0x3c0
	v_lshlrev_b32_e32 v9, 2, v210
	v_and_or_b32 v7, v7, s2, v8
	v_and_b32_e32 v9, 32, v9
	v_readlane_b32 s2, v249, 42
	v_lshlrev_b32_e32 v0, 2, v0
	v_lshl_or_b32 v1, v1, 6, v8
	v_bitop3_b32 v7, v7, s2, v9 bitop3:0xde
	v_and_b32_e32 v0, 32, v0
	v_readlane_b32 s2, v249, 44
	v_mov_b32_e32 v199, v65
	v_mov_b32_e32 v203, v65
	v_bitop3_b32 v8, v1, s2, v0 bitop3:0xde
	s_add_u32 s2, s14, 0x40000
	s_addc_u32 s3, s15, 0
	s_add_i32 s42, s13, 0x18000
	v_lshl_add_u64 v[0:1], s[2:3], 0, v[64:65]
	s_mov_b32 m0, s42
	s_add_i32 s43, s13, 0x1a000
	v_lshl_add_u64 v[2:3], s[16:17], 0, v[202:203]
	v_mov_b32_e32 v197, v65
	s_waitcnt vmcnt(2)
	s_barrier
	global_load_lds_dwordx4 v[0:1], off
	v_lshl_add_u64 v[0:1], s[2:3], 0, v[198:199]
	s_mov_b32 m0, s43
	s_add_i32 s44, s13, 0x8000
	s_add_i32 s45, s13, 0xa000
	v_lshl_add_u64 v[4:5], s[16:17], 0, v[196:197]
	global_load_lds_dwordx4 v[0:1], off
	v_lshl_add_u64 v[0:1], v[2:3], 0, s[94:95]
	s_mov_b32 m0, s44
	s_add_u32 s2, s14, 0x40200
	global_load_lds_dwordx4 v[0:1], off
	v_lshl_add_u64 v[0:1], v[4:5], 0, s[94:95]
	s_mov_b32 m0, s45
	s_addc_u32 s3, s15, 0
	s_add_i32 s46, s13, 0x1c000
	global_load_lds_dwordx4 v[0:1], off
	v_lshl_add_u64 v[216:217], s[2:3], 0, v[64:65]
	s_add_i32 s47, s13, 0x1e000
	v_lshl_add_u64 v[218:219], s[2:3], 0, v[198:199]
	v_readlane_b32 s2, v249, 43
	s_waitcnt vmcnt(4)
	s_nop 0
	v_or_b32_e32 v204, s2, v6
	v_readlane_b32 s2, v251, 41
	v_mov_b32_e32 v201, v65
	v_mov_b32_e32 v195, v65
	v_mov_b32_e32 v205, v65
	s_mov_b32 s48, 0
	s_mov_b64 s[18:19], 0
	v_add_u32_e32 v211, 0, v8
	v_add_u32_e32 v212, 0, v7
	s_mov_b32 s49, s2
	s_mov_b64 s[8:9], s[14:15]
	s_mov_b64 s[10:11], s[16:17]
	s_barrier
	v_readlane_b32 s3, v251, 42
	s_branch .LBB0_1407

; #define PG8_STAGE_B(bufoff, gbase) do { _Pragma("unroll") for (int _i = 0; _i < 2; ++_i) \
;         __builtin_amdgcn_global_load_lds((const unsigned*)((const char*)(gbase) + voffB[_i]), (LAS unsigned*)(lds + (bufoff) + ldsw + _i * 8192), 16, 0, 0); } while (0)
; #define PG8_STAGE_A(bufoff, gbase, VO, h) do { _Pragma("unroll") for (int _i = 0; _i < 2; ++_i) \
;         __builtin_amdgcn_global_load_lds((const unsigned*)((const char*)(gbase) + (VO)[h][_i]), (LAS unsigned*)(lds + (bufoff) + ldsw + _i * 8192), 16, 0, 0); } while (0)
; #define PG8_WAIT_V(n) asm volatile("s_waitcnt vmcnt(" #n ")" ::: "memory")
; #define PG8_WAIT_L(n) asm volatile("s_waitcnt lgkmcnt(" #n ")" ::: "memory")
; #define PG8_WAIT_VX(rx) do { if (rx) asm volatile("s_waitcnt vmcnt(%0)" :: "n"(8 + Epi::NVM) : "memory"); else asm volatile("s_waitcnt vmcnt(8)" ::: "memory"); } while (0)
; #define PG8_BAR __builtin_amdgcn_s_barrier()
; #define PG8_SCHED __builtin_amdgcn_sched_barrier(0)
;     ...
;             PG8_WAIT_VX(rx); PG8_WAIT_L(0); PG8_BAR; PG8_MMA(0, 0, At, B0); PG8_MMA(0, 1, At, B1); PG8_BAR; PG8_SCHED;
;             PG8_LDA(At, 1, 1); PG8_STAGE_B(PG8_SB(1, 0), b3); PG8_STAGE_B(PG8_SB(1, 1), b3 + hstepB); PG8_STAGE_A(PG8_SA(1, 0), a3, vo2, 0);
;             PG8_WAIT_V(8); PG8_WAIT_L(0); PG8_BAR; PG8_MMA(1, 0, At, B0); PG8_MMA(1, 1, At, B1); PG8_BAR; PG8_SCHED;
.LBB0_1410:
	s_xor_b64 s[26:27], s[22:23], -1
	s_waitcnt lgkmcnt(0)
	s_add_u32 s2, s24, 0x40000
	s_addc_u32 s3, s25, 0
	s_barrier
	s_setprio 1
	s_waitcnt lgkmcnt(0)
	v_mfma_scale_f32_16x16x128_f8f6f4 v[190:193], v[24:31], v[56:63], v[190:193], v226, v228 op_sel_hi:[0,0,0]
	v_mfma_scale_f32_16x16x128_f8f6f4 v[186:189], v[16:23], v[56:63], v[186:189], v226, v228 op_sel_hi:[0,0,0]
	v_mfma_scale_f32_16x16x128_f8f6f4 v[178:181], v[24:31], v[48:55], v[178:181], v226, v228 op_sel_hi:[0,0,0]
	v_mfma_scale_f32_16x16x128_f8f6f4 v[170:173], v[16:23], v[48:55], v[170:173], v226, v228 op_sel_hi:[0,0,0]
	v_mfma_scale_f32_16x16x128_f8f6f4 v[162:165], v[24:31], v[40:47], v[162:165], v226, v228 op_sel_hi:[0,0,0]
	v_mfma_scale_f32_16x16x128_f8f6f4 v[154:157], v[16:23], v[40:47], v[154:157], v226, v228 op_sel_hi:[0,0,0]
	v_mfma_scale_f32_16x16x128_f8f6f4 v[146:149], v[24:31], v[32:39], v[146:149], v226, v228 op_sel_hi:[0,0,0]
	v_mfma_scale_f32_16x16x128_f8f6f4 v[138:141], v[16:23], v[32:39], v[138:141], v226, v228 op_sel_hi:[0,0,0]
	s_setprio 0
	s_setprio 1
	v_mfma_scale_f32_16x16x128_f8f6f4 v[182:185], v[8:15], v[56:63], v[182:185], v226, v228 op_sel_hi:[0,0,0]
	v_mfma_scale_f32_16x16x128_f8f6f4 v[174:177], v[0:7], v[56:63], v[174:177], v226, v228 op_sel_hi:[0,0,0]
	v_mfma_scale_f32_16x16x128_f8f6f4 v[166:169], v[8:15], v[48:55], v[166:169], v226, v228 op_sel_hi:[0,0,0]
	v_mfma_scale_f32_16x16x128_f8f6f4 v[158:161], v[0:7], v[48:55], v[158:161], v226, v228 op_sel_hi:[0,0,0]
	v_mfma_scale_f32_16x16x128_f8f6f4 v[150:153], v[8:15], v[40:47], v[150:153], v226, v228 op_sel_hi:[0,0,0]
	v_mfma_scale_f32_16x16x128_f8f6f4 v[142:145], v[0:7], v[40:47], v[142:145], v226, v228 op_sel_hi:[0,0,0]
	v_mfma_scale_f32_16x16x128_f8f6f4 v[134:137], v[8:15], v[32:39], v[134:137], v226, v228 op_sel_hi:[0,0,0]
	v_mfma_scale_f32_16x16x128_f8f6f4 v[130:133], v[0:7], v[32:39], v[130:133], v226, v228 op_sel_hi:[0,0,0]
	s_setprio 0
	s_barrier
	s_mov_b32 m0, s42
	v_lshl_add_u64 v[214:215], s[2:3], 0, v[64:65]
	ds_read_b128 v[32:35], v212 offset:49152
	ds_read_b128 v[36:39], v212 offset:50176
	ds_read_b128 v[40:43], v212 offset:51200
	ds_read_b128 v[44:47], v212 offset:52224
	ds_read_b128 v[48:51], v212 offset:53248
	ds_read_b128 v[52:55], v212 offset:54272
	ds_read_b128 v[56:59], v212 offset:55296
	ds_read_b128 v[60:63], v212 offset:56320
	global_load_lds_dwordx4 v[214:215], off
	v_lshl_add_u64 v[214:215], s[2:3], 0, v[198:199]
	s_add_u32 s2, s24, 0x40200
	s_mov_b32 m0, s43
	s_addc_u32 s3, s25, 0
	global_load_lds_dwordx4 v[214:215], off
	v_lshl_add_u64 v[216:217], s[2:3], 0, v[64:65]
	v_lshl_add_u64 v[206:207], v[206:207], 0, s[94:95]
	v_lshl_add_u64 v[218:219], s[2:3], 0, v[198:199]
	s_mov_b32 m0, s44
	s_nop 0
	global_load_lds_dwordx4 v[206:207], off
	v_lshl_add_u64 v[206:207], v[208:209], 0, s[94:95]
	s_mov_b32 m0, s45
	s_nop 0
	global_load_lds_dwordx4 v[206:207], off
	s_waitcnt vmcnt(6)
	s_waitcnt lgkmcnt(0)
	s_barrier
	s_setprio 1
	s_waitcnt lgkmcnt(0)
	v_mfma_scale_f32_16x16x128_f8f6f4 v[126:129], v[24:31], v[32:39], v[126:129], v226, v228 op_sel_hi:[0,0,0]
	v_mfma_scale_f32_16x16x128_f8f6f4 v[122:125], v[16:23], v[32:39], v[122:125], v226, v228 op_sel_hi:[0,0,0]
	v_mfma_scale_f32_16x16x128_f8f6f4 v[114:117], v[24:31], v[40:47], v[114:117], v226, v228 op_sel_hi:[0,0,0]
	v_mfma_scale_f32_16x16x128_f8f6f4 v[106:109], v[16:23], v[40:47], v[106:109], v226, v228 op_sel_hi:[0,0,0]
	v_mfma_scale_f32_16x16x128_f8f6f4 v[90:93], v[24:31], v[48:55], v[90:93], v226, v228 op_sel_hi:[0,0,0]
	v_mfma_scale_f32_16x16x128_f8f6f4 v[82:85], v[16:23], v[48:55], v[82:85], v226, v228 op_sel_hi:[0,0,0]
	v_mfma_scale_f32_16x16x128_f8f6f4 v[70:73], v[24:31], v[56:63], v[70:73], v226, v228 op_sel_hi:[0,0,0]
	v_mfma_scale_f32_16x16x128_f8f6f4 v[66:69], v[16:23], v[56:63], v[66:69], v226, v228 op_sel_hi:[0,0,0]
	s_setprio 0
	s_setprio 1
	v_mfma_scale_f32_16x16x128_f8f6f4 v[118:121], v[8:15], v[32:39], v[118:121], v226, v228 op_sel_hi:[0,0,0]
	v_mfma_scale_f32_16x16x128_f8f6f4 v[110:113], v[0:7], v[32:39], v[110:113], v226, v228 op_sel_hi:[0,0,0]
	v_mfma_scale_f32_16x16x128_f8f6f4 v[94:97], v[8:15], v[40:47], v[94:97], v226, v228 op_sel_hi:[0,0,0]
	v_mfma_scale_f32_16x16x128_f8f6f4 v[86:89], v[0:7], v[40:47], v[86:89], v226, v228 op_sel_hi:[0,0,0]
	v_mfma_scale_f32_16x16x128_f8f6f4 v[102:105], v[8:15], v[48:55], v[102:105], v226, v228 op_sel_hi:[0,0,0]
	v_mfma_scale_f32_16x16x128_f8f6f4 v[98:101], v[0:7], v[48:55], v[98:101], v226, v228 op_sel_hi:[0,0,0]
	v_mfma_scale_f32_16x16x128_f8f6f4 v[78:81], v[8:15], v[56:63], v[78:81], v226, v228 op_sel_hi:[0,0,0]
	v_mfma_scale_f32_16x16x128_f8f6f4 v[74:77], v[0:7], v[56:63], v[74:77], v226, v228 op_sel_hi:[0,0,0]
	s_setprio 0
	s_barrier
	s_mov_b32 s5, 2
	s_mov_b64 s[22:23], 0
	s_mov_b64 s[2:3], -1
	s_and_b64 vcc, exec, s[26:27]
	s_cbranch_vccnz .LBB0_1423

; #define PG8_STAGE_B(bufoff, gbase) do { _Pragma("unroll") for (int _i = 0; _i < 2; ++_i) \
;         __builtin_amdgcn_global_load_lds((const unsigned*)((const char*)(gbase) + voffB[_i]), (LAS unsigned*)(lds + (bufoff) + ldsw + _i * 8192), 16, 0, 0); } while (0)
; #define PG8_STAGE_A(bufoff, gbase, VO, h) do { _Pragma("unroll") for (int _i = 0; _i < 2; ++_i) \
;         __builtin_amdgcn_global_load_lds((const unsigned*)((const char*)(gbase) + (VO)[h][_i]), (LAS unsigned*)(lds + (bufoff) + ldsw + _i * 8192), 16, 0, 0); } while (0)
; #define PG8_WAIT_L(n) asm volatile("s_waitcnt lgkmcnt(" #n ")" ::: "memory")
; #define PG8_WAIT_VX(rx) do { if (rx) asm volatile("s_waitcnt vmcnt(%0)" :: "n"(8 + Epi::NVM) : "memory"); else asm volatile("s_waitcnt vmcnt(8)" ::: "memory"); } while (0)
; #define PG8_BAR __builtin_amdgcn_s_barrier()
; #define PG8_SCHED __builtin_amdgcn_sched_barrier(0)
;     ...
;             PG8_LDB(B0, 0, 0); PG8_LDB(B1, 0, 1); PG8_SCHED; PG8_LDA(At, 0, 0); if (!rx) PG8_STAGE_A(PG8_SA(1, 1), a1, voffA, 1);
;             PG8_WAIT_VX(rx); PG8_WAIT_L(0); PG8_BAR; PG8_MMA(0, 0, At, B0); PG8_MMA(0, 1, At, B1); PG8_BAR; PG8_SCHED;
;             PG8_LDA(At, 0, 1); PG8_STAGE_B(PG8_SB(0, 0), b2); PG8_STAGE_B(PG8_SB(0, 1), b2 + hstepB); PG8_STAGE_A(PG8_SA(0, 0), a2, vo2, 0);
.LBB0_1413:
	s_andn2_b64 vcc, exec, s[26:27]
	s_cbranch_vccnz .LBB0_1415
	s_mov_b32 m0, s46
	s_nop 0
	global_load_lds_dwordx4 v[216:217], off
	s_mov_b32 m0, s47
	s_nop 0
	global_load_lds_dwordx4 v[218:219], off
	v_lshl_add_u64 v[206:207], s[24:25], 0, v[200:201]
	v_lshl_add_u64 v[206:207], v[206:207], 0, s[94:95]
	s_add_i32 m0, s13, 0xc000
	s_nop 0
	global_load_lds_dwordx4 v[206:207], off
	v_lshl_add_u64 v[206:207], s[24:25], 0, v[194:195]
	v_lshl_add_u64 v[206:207], v[206:207], 0, s[94:95]
	s_add_i32 m0, s13, 0xe000
	s_nop 0
	global_load_lds_dwordx4 v[206:207], off
	s_waitcnt vmcnt(8)
.LBB0_1415:
	s_add_u32 s7, s24, 0x100
	s_addc_u32 s26, s25, 0
	s_and_b64 s[24:25], s[2:3], exec
	s_cselect_b32 s27, s11, s26
	s_cselect_b32 s26, s10, s7
	s_lshl_b32 s5, s5, 18
	s_add_u32 s5, s14, s5
	s_addc_u32 s7, s15, 0
	s_add_u32 s5, s5, 0x80000
	s_addc_u32 s7, s7, 0
	s_waitcnt lgkmcnt(0)
	s_and_b64 s[2:3], s[2:3], exec
	s_cselect_b32 s25, s9, s7
	s_cselect_b32 s24, s8, s5
	s_barrier
	s_setprio 1
	s_waitcnt lgkmcnt(0)
	v_mfma_scale_f32_16x16x128_f8f6f4 v[190:193], v[24:31], v[56:63], v[190:193], v226, v228 op_sel_hi:[0,0,0]
	v_mfma_scale_f32_16x16x128_f8f6f4 v[186:189], v[16:23], v[56:63], v[186:189], v226, v228 op_sel_hi:[0,0,0]
	v_mfma_scale_f32_16x16x128_f8f6f4 v[178:181], v[24:31], v[48:55], v[178:181], v226, v228 op_sel_hi:[0,0,0]
	v_mfma_scale_f32_16x16x128_f8f6f4 v[170:173], v[16:23], v[48:55], v[170:173], v226, v228 op_sel_hi:[0,0,0]
	v_mfma_scale_f32_16x16x128_f8f6f4 v[162:165], v[24:31], v[40:47], v[162:165], v226, v228 op_sel_hi:[0,0,0]
	v_mfma_scale_f32_16x16x128_f8f6f4 v[154:157], v[16:23], v[40:47], v[154:157], v226, v228 op_sel_hi:[0,0,0]
	v_mfma_scale_f32_16x16x128_f8f6f4 v[146:149], v[24:31], v[32:39], v[146:149], v226, v228 op_sel_hi:[0,0,0]
	v_mfma_scale_f32_16x16x128_f8f6f4 v[138:141], v[16:23], v[32:39], v[138:141], v226, v228 op_sel_hi:[0,0,0]
	s_setprio 0
	s_setprio 1
	v_mfma_scale_f32_16x16x128_f8f6f4 v[182:185], v[8:15], v[56:63], v[182:185], v226, v228 op_sel_hi:[0,0,0]
	v_mfma_scale_f32_16x16x128_f8f6f4 v[174:177], v[0:7], v[56:63], v[174:177], v226, v228 op_sel_hi:[0,0,0]
	v_mfma_scale_f32_16x16x128_f8f6f4 v[166:169], v[8:15], v[48:55], v[166:169], v226, v228 op_sel_hi:[0,0,0]
	v_mfma_scale_f32_16x16x128_f8f6f4 v[158:161], v[0:7], v[48:55], v[158:161], v226, v228 op_sel_hi:[0,0,0]
	v_mfma_scale_f32_16x16x128_f8f6f4 v[150:153], v[8:15], v[40:47], v[150:153], v226, v228 op_sel_hi:[0,0,0]
	v_mfma_scale_f32_16x16x128_f8f6f4 v[142:145], v[0:7], v[40:47], v[142:145], v226, v228 op_sel_hi:[0,0,0]
	v_mfma_scale_f32_16x16x128_f8f6f4 v[134:137], v[8:15], v[32:39], v[134:137], v226, v228 op_sel_hi:[0,0,0]
	v_mfma_scale_f32_16x16x128_f8f6f4 v[130:133], v[0:7], v[32:39], v[130:133], v226, v228 op_sel_hi:[0,0,0]
	s_setprio 0
	s_barrier
	s_mov_b32 m0, s35
	v_lshl_add_u64 v[206:207], s[24:25], 0, v[64:65]
	s_add_u32 s2, s24, 0x200
	ds_read_b128 v[56:59], v212 offset:16384
	ds_read_b128 v[60:63], v212 offset:17408
	ds_read_b128 v[48:51], v212 offset:18432
	ds_read_b128 v[52:55], v212 offset:19456
	ds_read_b128 v[40:43], v212 offset:20480
	ds_read_b128 v[44:47], v212 offset:21504
	ds_read_b128 v[32:35], v212 offset:22528
	ds_read_b128 v[36:39], v212 offset:23552
	global_load_lds_dwordx4 v[206:207], off
	v_lshl_add_u64 v[206:207], s[24:25], 0, v[198:199]
	s_mov_b32 m0, s36
	s_addc_u32 s3, s25, 0
	global_load_lds_dwordx4 v[206:207], off
	v_lshl_add_u64 v[216:217], s[2:3], 0, v[64:65]
	v_lshl_add_u64 v[208:209], s[26:27], 0, v[196:197]
	v_lshl_add_u64 v[218:219], s[2:3], 0, v[198:199]
	v_cndmask_b32_e64 v213, 0, 1, s[28:29]
	v_lshl_add_u64 v[206:207], s[26:27], 0, v[202:203]
	s_mov_b32 m0, s13
	v_cmp_ne_u32_e64 s[2:3], 1, v213
	global_load_lds_dwordx4 v[206:207], off
	s_mov_b32 m0, s39
	s_andn2_b64 vcc, exec, s[28:29]
	global_load_lds_dwordx4 v[208:209], off
	s_cbranch_vccnz .LBB0_1420
	s_waitcnt vmcnt(14)
	s_cbranch_execnz .LBB0_1418

; #define PG8_STAGE_A(bufoff, gbase, VO, h) do { _Pragma("unroll") for (int _i = 0; _i < 2; ++_i) \
;         __builtin_amdgcn_global_load_lds((const unsigned*)((const char*)(gbase) + (VO)[h][_i]), (LAS unsigned*)(lds + (bufoff) + ldsw + _i * 8192), 16, 0, 0); } while (0)
; #define PG8_WAIT_L(n) asm volatile("s_waitcnt lgkmcnt(" #n ")" ::: "memory")
; #define PG8_WAIT_VX(rx) do { if (rx) asm volatile("s_waitcnt vmcnt(%0)" :: "n"(8 + Epi::NVM) : "memory"); else asm volatile("s_waitcnt vmcnt(8)" ::: "memory"); } while (0)
; #define PG8_BAR __builtin_amdgcn_s_barrier()
; #define PG8_SCHED __builtin_amdgcn_sched_barrier(0)
;     ...
;             PG8_WAIT_VX(rx); PG8_WAIT_L(0); PG8_BAR; PG8_MMA(1, 0, At, B0); PG8_MMA(1, 1, At, B1); PG8_BAR; PG8_SCHED;
;             PG8_LDB(B0, 1, 0); PG8_LDB(B1, 1, 1); PG8_SCHED; PG8_LDA(At, 1, 0); PG8_STAGE_A(PG8_SA(0, 1), a2, vo2, 1);
.LBB0_1418:
	s_waitcnt lgkmcnt(0)
	s_barrier
	s_setprio 1
	s_waitcnt lgkmcnt(0)
	v_mfma_scale_f32_16x16x128_f8f6f4 v[126:129], v[24:31], v[56:63], v[126:129], v226, v228 op_sel_hi:[0,0,0]
	v_mfma_scale_f32_16x16x128_f8f6f4 v[122:125], v[16:23], v[56:63], v[122:125], v226, v228 op_sel_hi:[0,0,0]
	v_mfma_scale_f32_16x16x128_f8f6f4 v[114:117], v[24:31], v[48:55], v[114:117], v226, v228 op_sel_hi:[0,0,0]
	v_mfma_scale_f32_16x16x128_f8f6f4 v[106:109], v[16:23], v[48:55], v[106:109], v226, v228 op_sel_hi:[0,0,0]
	v_mfma_scale_f32_16x16x128_f8f6f4 v[90:93], v[24:31], v[40:47], v[90:93], v226, v228 op_sel_hi:[0,0,0]
	v_mfma_scale_f32_16x16x128_f8f6f4 v[82:85], v[16:23], v[40:47], v[82:85], v226, v228 op_sel_hi:[0,0,0]
	v_mfma_scale_f32_16x16x128_f8f6f4 v[70:73], v[24:31], v[32:39], v[70:73], v226, v228 op_sel_hi:[0,0,0]
	v_mfma_scale_f32_16x16x128_f8f6f4 v[66:69], v[16:23], v[32:39], v[66:69], v226, v228 op_sel_hi:[0,0,0]
	s_setprio 0
	s_setprio 1
	v_mfma_scale_f32_16x16x128_f8f6f4 v[118:121], v[8:15], v[56:63], v[118:121], v226, v228 op_sel_hi:[0,0,0]
	v_mfma_scale_f32_16x16x128_f8f6f4 v[110:113], v[0:7], v[56:63], v[110:113], v226, v228 op_sel_hi:[0,0,0]
	v_mfma_scale_f32_16x16x128_f8f6f4 v[94:97], v[8:15], v[48:55], v[94:97], v226, v228 op_sel_hi:[0,0,0]
	v_mfma_scale_f32_16x16x128_f8f6f4 v[86:89], v[0:7], v[48:55], v[86:89], v226, v228 op_sel_hi:[0,0,0]
	v_mfma_scale_f32_16x16x128_f8f6f4 v[102:105], v[8:15], v[40:47], v[102:105], v226, v228 op_sel_hi:[0,0,0]
	v_mfma_scale_f32_16x16x128_f8f6f4 v[98:101], v[0:7], v[40:47], v[98:101], v226, v228 op_sel_hi:[0,0,0]
	v_mfma_scale_f32_16x16x128_f8f6f4 v[78:81], v[8:15], v[32:39], v[78:81], v226, v228 op_sel_hi:[0,0,0]
	v_mfma_scale_f32_16x16x128_f8f6f4 v[74:77], v[0:7], v[32:39], v[74:77], v226, v228 op_sel_hi:[0,0,0]
	s_setprio 0
	s_barrier
	v_add_u32_e32 v0, 0x18000, v211
	v_add_u32_e32 v4, 0x1c000, v211
	ds_read_b128 v[24:27], v0
	ds_read_b128 v[28:31], v0 offset:1024
	ds_read_b128 v[16:19], v0 offset:2048
	ds_read_b128 v[20:23], v0 offset:3072
	ds_read_b128 v[8:11], v4
	ds_read_b128 v[12:15], v4 offset:1024
	ds_read_b128 v[0:3], v4 offset:2048
	ds_read_b128 v[4:7], v4 offset:3072
	s_mov_b32 m0, s40
	v_lshl_add_u64 v[214:215], s[26:27], 0, v[200:201]
	ds_read_b128 v[56:59], v212 offset:32768
	ds_read_b128 v[60:63], v212 offset:33792
	ds_read_b128 v[48:51], v212 offset:34816
	ds_read_b128 v[52:55], v212 offset:35840
	ds_read_b128 v[40:43], v212 offset:36864
	ds_read_b128 v[44:47], v212 offset:37888
	ds_read_b128 v[32:35], v212 offset:38912
	ds_read_b128 v[36:39], v212 offset:39936
	s_mov_b32 m0, s37
	s_nop 0
	global_load_lds_dwordx4 v[216:217], off
	s_mov_b32 m0, s38
	s_nop 0
	global_load_lds_dwordx4 v[218:219], off
	s_mov_b32 m0, s40
	s_nop 0
	global_load_lds_dwordx4 v[214:215], off
	v_lshl_add_u64 v[214:215], s[26:27], 0, v[194:195]
	s_mov_b32 m0, s41
	s_and_b64 vcc, exec, s[2:3]
	global_load_lds_dwordx4 v[214:215], off
	s_cbranch_vccnz .LBB0_1421
	s_waitcnt vmcnt(16)
	s_cbranch_execnz .LBB0_1410
	s_branch .LBB0_1422

; #define PG8_STAGE_A(bufoff, gbase, VO, h) do { _Pragma("unroll") for (int _i = 0; _i < 2; ++_i) \
;         __builtin_amdgcn_global_load_lds((const unsigned*)((const char*)(gbase) + (VO)[h][_i]), (LAS unsigned*)(lds + (bufoff) + ldsw + _i * 8192), 16, 0, 0); } while (0)
; #define PG8_BAR __builtin_amdgcn_s_barrier()
;     ...
;         if (ALIGN_EPI) { if (wr == 0) PG8_BAR; }
;         if (ALIGN_EPI && has_next) { if constexpr (GATHER) PG8_STAGE_A(PG8_SA(1, 1), nA + kstep, voffN, 1); else PG8_STAGE_A(PG8_SA(1, 1), nA + kstep, voffA, 1); }
.LBB0_1425:
	v_cndmask_b32_e64 v0, 0, 1, s[20:21]
	v_cmp_ne_u32_e64 s[2:3], 1, v0
	s_andn2_b64 vcc, exec, s[20:21]
	s_cbranch_vccnz .LBB0_1427
	v_lshl_add_u64 v[2:3], s[10:11], 0, v[200:201]
	v_lshl_add_u64 v[0:1], s[10:11], 0, v[194:195]
	v_lshl_add_u64 v[2:3], v[2:3], 0, s[94:95]
	s_mov_b32 m0, s46
	s_nop 0
	global_load_lds_dwordx4 v[216:217], off
	s_mov_b32 m0, s47
	s_nop 0
	global_load_lds_dwordx4 v[218:219], off
	s_add_i32 m0, s13, 0xc000
	v_lshl_add_u64 v[0:1], v[0:1], 0, s[94:95]
	global_load_lds_dwordx4 v[2:3], off
	s_add_i32 m0, s13, 0xe000
	s_nop 0
	global_load_lds_dwordx4 v[0:1], off
